# radix descent: tie walk starts at index bit 12 (bits 15..13 always set) and every descent loop exits as soon as a candidate is met by exactly 256 entries (on top of v49)
# speedup vs baseline: 1.0098x; 1.0095x over previous
.LBB0_821:
	s_add_i32 s0, s0, -1
	s_lshl_b32 s1, 1, s0
	s_or_b32 s1, s1, s9
	s_waitcnt lgkmcnt(0)
	v_cmp_le_u32_e64 s[14:15], s1, v90
	v_cmp_le_u32_e64 s[16:17], s1, v88
	v_cmp_le_u32_e64 s[18:19], s1, v89
	v_cmp_le_u32_e64 s[20:21], s1, v86
	v_cmp_le_u32_e64 s[22:23], s1, v87
	v_cmp_le_u32_e64 s[24:25], s1, v84
	v_cmp_le_u32_e64 s[26:27], s1, v85
	v_cmp_le_u32_e64 s[28:29], s1, v82
	v_cmp_le_u32_e64 s[30:31], s1, v83
	v_cmp_le_u32_e64 s[34:35], s1, v80
	v_cmp_le_u32_e64 s[36:37], s1, v81
	v_cmp_le_u32_e64 s[38:39], s1, v9
	s_bcnt1_i32_b64 s11, s[14:15]
	s_bcnt1_i32_b64 s12, s[16:17]
	s_add_i32 s11, s11, s12
	s_bcnt1_i32_b64 s12, s[18:19]
	s_add_i32 s11, s11, s12
	s_bcnt1_i32_b64 s12, s[20:21]
	s_add_i32 s11, s11, s12
	s_bcnt1_i32_b64 s12, s[22:23]
	s_add_i32 s11, s11, s12
	s_bcnt1_i32_b64 s12, s[24:25]
	s_add_i32 s11, s11, s12
	v_cmp_le_u32_e64 s[14:15], s1, v78
	v_cmp_le_u32_e64 s[16:17], s1, v7
	v_cmp_le_u32_e64 s[18:19], s1, v8
	v_cmp_le_u32_e64 s[20:21], s1, v5
	v_cmp_le_u32_e64 s[22:23], s1, v6
	v_cmp_le_u32_e64 s[24:25], s1, v3
	s_bcnt1_i32_b64 s12, s[26:27]
	s_add_i32 s11, s11, s12
	s_bcnt1_i32_b64 s12, s[28:29]
	s_add_i32 s11, s11, s12
	s_bcnt1_i32_b64 s12, s[30:31]
	s_add_i32 s11, s11, s12
	s_bcnt1_i32_b64 s12, s[34:35]
	s_add_i32 s11, s11, s12
	s_bcnt1_i32_b64 s12, s[36:37]
	s_add_i32 s11, s11, s12
	s_bcnt1_i32_b64 s12, s[38:39]
	s_add_i32 s11, s11, s12
	v_cmp_le_u32_e64 s[26:27], s1, v4
	v_cmp_le_u32_e64 s[28:29], s1, v2
	s_bcnt1_i32_b64 s12, s[14:15]
	s_add_i32 s11, s11, s12
	s_bcnt1_i32_b64 s12, s[16:17]
	s_add_i32 s11, s11, s12
	s_bcnt1_i32_b64 s12, s[18:19]
	s_add_i32 s11, s11, s12
	s_bcnt1_i32_b64 s12, s[20:21]
	s_add_i32 s11, s11, s12
	s_bcnt1_i32_b64 s12, s[22:23]
	s_add_i32 s11, s11, s12
	s_bcnt1_i32_b64 s12, s[24:25]
	s_add_i32 s11, s11, s12
	s_bcnt1_i32_b64 s12, s[26:27]
	s_add_i32 s11, s11, s12
	s_bcnt1_i32_b64 s12, s[28:29]
	s_add_i32 s11, s11, s12
	s_cmpk_gt_u32 s11, 0xff
	s_cselect_b32 s9, s1, s9
	s_cmpk_eq_i32 s11, 0x100
	s_cbranch_scc1 .LBB0_825
	s_cmp_lt_u32 s0, 17
	s_cbranch_scc0 .LBB0_821
	v_cmp_le_u32_e64 s[14:15], s9, v90
	v_cmp_le_u32_e64 s[16:17], s9, v88
	v_cmp_le_u32_e64 s[18:19], s9, v89
	v_cmp_le_u32_e64 s[20:21], s9, v86
	v_cmp_le_u32_e64 s[22:23], s9, v87
	v_cmp_le_u32_e64 s[24:25], s9, v84
	v_cmp_le_u32_e64 s[26:27], s9, v85
	v_cmp_le_u32_e64 s[28:29], s9, v82
	v_cmp_le_u32_e64 s[30:31], s9, v83
	v_cmp_le_u32_e64 s[34:35], s9, v80
	v_cmp_le_u32_e64 s[36:37], s9, v81
	v_cmp_le_u32_e64 s[38:39], s9, v9
	s_bcnt1_i32_b64 s0, s[14:15]
	s_bcnt1_i32_b64 s1, s[16:17]
	s_add_i32 s0, s0, s1
	s_bcnt1_i32_b64 s1, s[18:19]
	s_add_i32 s0, s0, s1
	s_bcnt1_i32_b64 s1, s[20:21]
	s_add_i32 s0, s0, s1
	s_bcnt1_i32_b64 s1, s[22:23]
	s_add_i32 s0, s0, s1
	s_bcnt1_i32_b64 s1, s[24:25]
	s_add_i32 s0, s0, s1
	v_cmp_le_u32_e64 s[14:15], s9, v78
	v_cmp_le_u32_e64 s[16:17], s9, v7
	v_cmp_le_u32_e64 s[18:19], s9, v8
	v_cmp_le_u32_e64 s[20:21], s9, v5
	v_cmp_le_u32_e64 s[22:23], s9, v6
	v_cmp_le_u32_e64 s[24:25], s9, v3
	s_bcnt1_i32_b64 s1, s[26:27]
	s_add_i32 s0, s0, s1
	s_bcnt1_i32_b64 s1, s[28:29]
	s_add_i32 s0, s0, s1
	s_bcnt1_i32_b64 s1, s[30:31]
	s_add_i32 s0, s0, s1
	s_bcnt1_i32_b64 s1, s[34:35]
	s_add_i32 s0, s0, s1
	s_bcnt1_i32_b64 s1, s[36:37]
	s_add_i32 s0, s0, s1
	s_bcnt1_i32_b64 s1, s[38:39]
	s_add_i32 s0, s0, s1
	v_cmp_le_u32_e64 s[26:27], s9, v4
	v_cmp_le_u32_e64 s[28:29], s9, v2
	s_bcnt1_i32_b64 s1, s[14:15]
	s_add_i32 s0, s0, s1
	s_bcnt1_i32_b64 s1, s[16:17]
	s_add_i32 s0, s0, s1
	s_bcnt1_i32_b64 s1, s[18:19]
	s_add_i32 s0, s0, s1
	s_bcnt1_i32_b64 s1, s[20:21]
	s_add_i32 s0, s0, s1
	s_bcnt1_i32_b64 s1, s[22:23]
	s_add_i32 s0, s0, s1
	s_bcnt1_i32_b64 s1, s[24:25]
	s_add_i32 s0, s0, s1
	s_bcnt1_i32_b64 s1, s[26:27]
	s_add_i32 s0, s0, s1
	s_bcnt1_i32_b64 s1, s[28:29]
	s_add_i32 s0, s0, s1
	s_cmpk_eq_i32 s0, 0x100
	s_cbranch_scc1 .LBB0_825
	s_or_b32 s9, s9, 0xe000
	s_mov_b32 s0, 12
.LBB0_824:
	s_lshl_b32 s1, 1, s0
	s_or_b32 s1, s1, s9
	v_cmp_le_u32_e64 s[14:15], s1, v90
	v_cmp_le_u32_e64 s[16:17], s1, v88
	v_cmp_le_u32_e64 s[18:19], s1, v89
	v_cmp_le_u32_e64 s[20:21], s1, v86
	v_cmp_le_u32_e64 s[22:23], s1, v87
	v_cmp_le_u32_e64 s[24:25], s1, v84
	v_cmp_le_u32_e64 s[26:27], s1, v85
	v_cmp_le_u32_e64 s[28:29], s1, v82
	v_cmp_le_u32_e64 s[30:31], s1, v83
	v_cmp_le_u32_e64 s[34:35], s1, v80
	v_cmp_le_u32_e64 s[36:37], s1, v81
	v_cmp_le_u32_e64 s[38:39], s1, v9
	s_bcnt1_i32_b64 s11, s[14:15]
	s_bcnt1_i32_b64 s12, s[16:17]
	s_add_i32 s11, s11, s12
	s_bcnt1_i32_b64 s12, s[18:19]
	s_add_i32 s11, s11, s12
	s_bcnt1_i32_b64 s12, s[20:21]
	s_add_i32 s11, s11, s12
	s_bcnt1_i32_b64 s12, s[22:23]
	s_add_i32 s11, s11, s12
	s_bcnt1_i32_b64 s12, s[24:25]
	s_add_i32 s11, s11, s12
	v_cmp_le_u32_e64 s[14:15], s1, v78
	v_cmp_le_u32_e64 s[16:17], s1, v7
	v_cmp_le_u32_e64 s[18:19], s1, v8
	v_cmp_le_u32_e64 s[20:21], s1, v5
	v_cmp_le_u32_e64 s[22:23], s1, v6
	v_cmp_le_u32_e64 s[24:25], s1, v3
	s_bcnt1_i32_b64 s12, s[26:27]
	s_add_i32 s11, s11, s12
	s_bcnt1_i32_b64 s12, s[28:29]
	s_add_i32 s11, s11, s12
	s_bcnt1_i32_b64 s12, s[30:31]
	s_add_i32 s11, s11, s12
	s_bcnt1_i32_b64 s12, s[34:35]
	s_add_i32 s11, s11, s12
	s_bcnt1_i32_b64 s12, s[36:37]
	s_add_i32 s11, s11, s12
	s_bcnt1_i32_b64 s12, s[38:39]
	s_add_i32 s11, s11, s12
	v_cmp_le_u32_e64 s[26:27], s1, v4
	v_cmp_le_u32_e64 s[28:29], s1, v2
	s_bcnt1_i32_b64 s12, s[14:15]
	s_add_i32 s11, s11, s12
	s_bcnt1_i32_b64 s12, s[16:17]
	s_add_i32 s11, s11, s12
	s_bcnt1_i32_b64 s12, s[18:19]
	s_add_i32 s11, s11, s12
	s_bcnt1_i32_b64 s12, s[20:21]
	s_add_i32 s11, s11, s12
	s_bcnt1_i32_b64 s12, s[22:23]
	s_add_i32 s11, s11, s12
	s_bcnt1_i32_b64 s12, s[24:25]
	s_add_i32 s11, s11, s12
	s_bcnt1_i32_b64 s12, s[26:27]
	s_add_i32 s11, s11, s12
	s_bcnt1_i32_b64 s12, s[28:29]
	s_add_i32 s11, s11, s12
	s_cmpk_gt_u32 s11, 0xff
	s_cselect_b32 s9, s1, s9
	s_cmpk_eq_i32 s11, 0x100
	s_cbranch_scc1 .LBB0_825
	s_add_i32 s0, s0, -1
	s_cmp_lg_u32 s0, -1
	s_cbranch_scc1 .LBB0_824

.LBB0_828:
	s_add_i32 s0, s0, -1
	s_lshl_b32 s1, 1, s0
	s_or_b32 s1, s1, s9
	s_waitcnt lgkmcnt(0)
	v_cmp_le_u32_e64 s[14:15], s1, v90
	v_cmp_le_u32_e64 s[16:17], s1, v88
	v_cmp_le_u32_e64 s[18:19], s1, v89
	v_cmp_le_u32_e64 s[20:21], s1, v86
	v_cmp_le_u32_e64 s[22:23], s1, v87
	v_cmp_le_u32_e64 s[24:25], s1, v84
	v_cmp_le_u32_e64 s[26:27], s1, v85
	v_cmp_le_u32_e64 s[28:29], s1, v82
	v_cmp_le_u32_e64 s[30:31], s1, v83
	v_cmp_le_u32_e64 s[34:35], s1, v80
	v_cmp_le_u32_e64 s[36:37], s1, v81
	v_cmp_le_u32_e64 s[38:39], s1, v9
	s_bcnt1_i32_b64 s11, s[14:15]
	s_bcnt1_i32_b64 s12, s[16:17]
	s_add_i32 s11, s11, s12
	s_bcnt1_i32_b64 s12, s[18:19]
	s_add_i32 s11, s11, s12
	s_bcnt1_i32_b64 s12, s[20:21]
	s_add_i32 s11, s11, s12
	s_bcnt1_i32_b64 s12, s[22:23]
	s_add_i32 s11, s11, s12
	s_bcnt1_i32_b64 s12, s[24:25]
	s_add_i32 s11, s11, s12
	v_cmp_le_u32_e64 s[14:15], s1, v78
	v_cmp_le_u32_e64 s[16:17], s1, v7
	v_cmp_le_u32_e64 s[18:19], s1, v8
	v_cmp_le_u32_e64 s[20:21], s1, v5
	s_bcnt1_i32_b64 s12, s[26:27]
	s_add_i32 s11, s11, s12
	s_bcnt1_i32_b64 s12, s[28:29]
	s_add_i32 s11, s11, s12
	s_bcnt1_i32_b64 s12, s[30:31]
	s_add_i32 s11, s11, s12
	s_bcnt1_i32_b64 s12, s[34:35]
	s_add_i32 s11, s11, s12
	s_bcnt1_i32_b64 s12, s[36:37]
	s_add_i32 s11, s11, s12
	s_bcnt1_i32_b64 s12, s[38:39]
	s_add_i32 s11, s11, s12
	s_bcnt1_i32_b64 s12, s[14:15]
	s_add_i32 s11, s11, s12
	s_bcnt1_i32_b64 s12, s[16:17]
	s_add_i32 s11, s11, s12
	s_bcnt1_i32_b64 s12, s[18:19]
	s_add_i32 s11, s11, s12
	s_bcnt1_i32_b64 s12, s[20:21]
	s_add_i32 s11, s11, s12
	s_cmpk_gt_u32 s11, 0xff
	s_cselect_b32 s9, s1, s9
	s_cmpk_eq_i32 s11, 0x100
	s_cbranch_scc1 .LBB0_832
	s_cmp_lt_u32 s0, 17
	s_cbranch_scc0 .LBB0_828
	v_cmp_le_u32_e64 s[14:15], s9, v90
	v_cmp_le_u32_e64 s[16:17], s9, v88
	v_cmp_le_u32_e64 s[18:19], s9, v89
	v_cmp_le_u32_e64 s[20:21], s9, v86
	v_cmp_le_u32_e64 s[22:23], s9, v87
	v_cmp_le_u32_e64 s[24:25], s9, v84
	v_cmp_le_u32_e64 s[26:27], s9, v85
	v_cmp_le_u32_e64 s[28:29], s9, v82
	v_cmp_le_u32_e64 s[30:31], s9, v83
	v_cmp_le_u32_e64 s[34:35], s9, v80
	v_cmp_le_u32_e64 s[36:37], s9, v81
	v_cmp_le_u32_e64 s[38:39], s9, v9
	s_bcnt1_i32_b64 s0, s[14:15]
	s_bcnt1_i32_b64 s1, s[16:17]
	s_add_i32 s0, s0, s1
	s_bcnt1_i32_b64 s1, s[18:19]
	s_add_i32 s0, s0, s1
	s_bcnt1_i32_b64 s1, s[20:21]
	s_add_i32 s0, s0, s1
	s_bcnt1_i32_b64 s1, s[22:23]
	s_add_i32 s0, s0, s1
	s_bcnt1_i32_b64 s1, s[24:25]
	s_add_i32 s0, s0, s1
	v_cmp_le_u32_e64 s[14:15], s9, v78
	v_cmp_le_u32_e64 s[16:17], s9, v7
	v_cmp_le_u32_e64 s[18:19], s9, v8
	v_cmp_le_u32_e64 s[20:21], s9, v5
	s_bcnt1_i32_b64 s1, s[26:27]
	s_add_i32 s0, s0, s1
	s_bcnt1_i32_b64 s1, s[28:29]
	s_add_i32 s0, s0, s1
	s_bcnt1_i32_b64 s1, s[30:31]
	s_add_i32 s0, s0, s1
	s_bcnt1_i32_b64 s1, s[34:35]
	s_add_i32 s0, s0, s1
	s_bcnt1_i32_b64 s1, s[36:37]
	s_add_i32 s0, s0, s1
	s_bcnt1_i32_b64 s1, s[38:39]
	s_add_i32 s0, s0, s1
	s_bcnt1_i32_b64 s1, s[14:15]
	s_add_i32 s0, s0, s1
	s_bcnt1_i32_b64 s1, s[16:17]
	s_add_i32 s0, s0, s1
	s_bcnt1_i32_b64 s1, s[18:19]
	s_add_i32 s0, s0, s1
	s_bcnt1_i32_b64 s1, s[20:21]
	s_add_i32 s0, s0, s1
	s_cmpk_eq_i32 s0, 0x100
	s_cbranch_scc1 .LBB0_832
	s_or_b32 s9, s9, 0xe000
	s_mov_b32 s0, 12
.LBB0_831:
	s_lshl_b32 s1, 1, s0
	s_or_b32 s1, s1, s9
	v_cmp_le_u32_e64 s[14:15], s1, v90
	v_cmp_le_u32_e64 s[16:17], s1, v88
	v_cmp_le_u32_e64 s[18:19], s1, v89
	v_cmp_le_u32_e64 s[20:21], s1, v86
	v_cmp_le_u32_e64 s[22:23], s1, v87
	v_cmp_le_u32_e64 s[24:25], s1, v84
	v_cmp_le_u32_e64 s[26:27], s1, v85
	v_cmp_le_u32_e64 s[28:29], s1, v82
	v_cmp_le_u32_e64 s[30:31], s1, v83
	v_cmp_le_u32_e64 s[34:35], s1, v80
	v_cmp_le_u32_e64 s[36:37], s1, v81
	v_cmp_le_u32_e64 s[38:39], s1, v9
	s_bcnt1_i32_b64 s11, s[14:15]
	s_bcnt1_i32_b64 s12, s[16:17]
	s_add_i32 s11, s11, s12
	s_bcnt1_i32_b64 s12, s[18:19]
	s_add_i32 s11, s11, s12
	s_bcnt1_i32_b64 s12, s[20:21]
	s_add_i32 s11, s11, s12
	s_bcnt1_i32_b64 s12, s[22:23]
	s_add_i32 s11, s11, s12
	s_bcnt1_i32_b64 s12, s[24:25]
	s_add_i32 s11, s11, s12
	v_cmp_le_u32_e64 s[14:15], s1, v78
	v_cmp_le_u32_e64 s[16:17], s1, v7
	v_cmp_le_u32_e64 s[18:19], s1, v8
	v_cmp_le_u32_e64 s[20:21], s1, v5
	s_bcnt1_i32_b64 s12, s[26:27]
	s_add_i32 s11, s11, s12
	s_bcnt1_i32_b64 s12, s[28:29]
	s_add_i32 s11, s11, s12
	s_bcnt1_i32_b64 s12, s[30:31]
	s_add_i32 s11, s11, s12
	s_bcnt1_i32_b64 s12, s[34:35]
	s_add_i32 s11, s11, s12
	s_bcnt1_i32_b64 s12, s[36:37]
	s_add_i32 s11, s11, s12
	s_bcnt1_i32_b64 s12, s[38:39]
	s_add_i32 s11, s11, s12
	s_bcnt1_i32_b64 s12, s[14:15]
	s_add_i32 s11, s11, s12
	s_bcnt1_i32_b64 s12, s[16:17]
	s_add_i32 s11, s11, s12
	s_bcnt1_i32_b64 s12, s[18:19]
	s_add_i32 s11, s11, s12
	s_bcnt1_i32_b64 s12, s[20:21]
	s_add_i32 s11, s11, s12
	s_cmpk_gt_u32 s11, 0xff
	s_cselect_b32 s9, s1, s9
	s_cmpk_eq_i32 s11, 0x100
	s_cbranch_scc1 .LBB0_832
	s_add_i32 s0, s0, -1
	s_cmp_eq_u32 s0, -1
	s_cbranch_scc0 .LBB0_831

.LBB0_875:
	s_add_i32 s0, s0, -1
	s_lshl_b32 s1, 1, s0
	s_or_b32 s1, s1, s10
	s_waitcnt lgkmcnt(0)
	v_cmp_le_u32_e64 s[14:15], s1, v90
	v_cmp_le_u32_e64 s[16:17], s1, v88
	v_cmp_le_u32_e64 s[18:19], s1, v89
	v_cmp_le_u32_e64 s[20:21], s1, v86
	v_cmp_le_u32_e64 s[22:23], s1, v87
	v_cmp_le_u32_e64 s[24:25], s1, v84
	v_cmp_le_u32_e64 s[26:27], s1, v85
	v_cmp_le_u32_e64 s[28:29], s1, v82
	v_cmp_le_u32_e64 s[30:31], s1, v83
	v_cmp_le_u32_e64 s[34:35], s1, v80
	v_cmp_le_u32_e64 s[36:37], s1, v81
	v_cmp_le_u32_e64 s[38:39], s1, v9
	s_bcnt1_i32_b64 s9, s[14:15]
	s_bcnt1_i32_b64 s11, s[16:17]
	s_add_i32 s9, s9, s11
	s_bcnt1_i32_b64 s11, s[18:19]
	s_add_i32 s9, s9, s11
	s_bcnt1_i32_b64 s11, s[20:21]
	s_add_i32 s9, s9, s11
	s_bcnt1_i32_b64 s11, s[22:23]
	s_add_i32 s9, s9, s11
	s_bcnt1_i32_b64 s11, s[24:25]
	s_add_i32 s9, s9, s11
	s_bcnt1_i32_b64 s11, s[26:27]
	s_add_i32 s9, s9, s11
	s_bcnt1_i32_b64 s11, s[28:29]
	s_add_i32 s9, s9, s11
	s_bcnt1_i32_b64 s11, s[30:31]
	s_add_i32 s9, s9, s11
	s_bcnt1_i32_b64 s11, s[34:35]
	s_add_i32 s9, s9, s11
	s_bcnt1_i32_b64 s11, s[36:37]
	s_add_i32 s9, s9, s11
	s_bcnt1_i32_b64 s11, s[38:39]
	s_add_i32 s9, s9, s11
	s_cmpk_gt_u32 s9, 0xff
	s_cselect_b32 s10, s1, s10
	s_cmpk_eq_i32 s9, 0x100
	s_cbranch_scc1 .LBB0_879
	s_cmp_lt_u32 s0, 17
	s_cbranch_scc0 .LBB0_875
	v_cmp_le_u32_e64 s[14:15], s10, v90
	v_cmp_le_u32_e64 s[16:17], s10, v88
	v_cmp_le_u32_e64 s[18:19], s10, v89
	v_cmp_le_u32_e64 s[20:21], s10, v86
	v_cmp_le_u32_e64 s[22:23], s10, v87
	v_cmp_le_u32_e64 s[24:25], s10, v84
	v_cmp_le_u32_e64 s[26:27], s10, v85
	v_cmp_le_u32_e64 s[28:29], s10, v82
	v_cmp_le_u32_e64 s[30:31], s10, v83
	v_cmp_le_u32_e64 s[34:35], s10, v80
	v_cmp_le_u32_e64 s[36:37], s10, v81
	v_cmp_le_u32_e64 s[38:39], s10, v9
	s_bcnt1_i32_b64 s0, s[14:15]
	s_bcnt1_i32_b64 s1, s[16:17]
	s_add_i32 s0, s0, s1
	s_bcnt1_i32_b64 s1, s[18:19]
	s_add_i32 s0, s0, s1
	s_bcnt1_i32_b64 s1, s[20:21]
	s_add_i32 s0, s0, s1
	s_bcnt1_i32_b64 s1, s[22:23]
	s_add_i32 s0, s0, s1
	s_bcnt1_i32_b64 s1, s[24:25]
	s_add_i32 s0, s0, s1
	s_bcnt1_i32_b64 s1, s[26:27]
	s_add_i32 s0, s0, s1
	s_bcnt1_i32_b64 s1, s[28:29]
	s_add_i32 s0, s0, s1
	s_bcnt1_i32_b64 s1, s[30:31]
	s_add_i32 s0, s0, s1
	s_bcnt1_i32_b64 s1, s[34:35]
	s_add_i32 s0, s0, s1
	s_bcnt1_i32_b64 s1, s[36:37]
	s_add_i32 s0, s0, s1
	s_bcnt1_i32_b64 s1, s[38:39]
	s_add_i32 s0, s0, s1
	s_cmpk_eq_i32 s0, 0x100
	s_cbranch_scc1 .LBB0_879
	s_or_b32 s10, s10, 0xe000
	s_mov_b32 s0, 12
.LBB0_878:
	s_lshl_b32 s1, 1, s0
	s_or_b32 s1, s1, s10
	v_cmp_le_u32_e64 s[14:15], s1, v90
	v_cmp_le_u32_e64 s[16:17], s1, v88
	v_cmp_le_u32_e64 s[18:19], s1, v89
	v_cmp_le_u32_e64 s[20:21], s1, v86
	v_cmp_le_u32_e64 s[22:23], s1, v87
	v_cmp_le_u32_e64 s[24:25], s1, v84
	v_cmp_le_u32_e64 s[26:27], s1, v85
	v_cmp_le_u32_e64 s[28:29], s1, v82
	v_cmp_le_u32_e64 s[30:31], s1, v83
	v_cmp_le_u32_e64 s[34:35], s1, v80
	v_cmp_le_u32_e64 s[36:37], s1, v81
	v_cmp_le_u32_e64 s[38:39], s1, v9
	s_bcnt1_i32_b64 s9, s[14:15]
	s_bcnt1_i32_b64 s11, s[16:17]
	s_add_i32 s9, s9, s11
	s_bcnt1_i32_b64 s11, s[18:19]
	s_add_i32 s9, s9, s11
	s_bcnt1_i32_b64 s11, s[20:21]
	s_add_i32 s9, s9, s11
	s_bcnt1_i32_b64 s11, s[22:23]
	s_add_i32 s9, s9, s11
	s_bcnt1_i32_b64 s11, s[24:25]
	s_add_i32 s9, s9, s11
	s_bcnt1_i32_b64 s11, s[26:27]
	s_add_i32 s9, s9, s11
	s_bcnt1_i32_b64 s11, s[28:29]
	s_add_i32 s9, s9, s11
	s_bcnt1_i32_b64 s11, s[30:31]
	s_add_i32 s9, s9, s11
	s_bcnt1_i32_b64 s11, s[34:35]
	s_add_i32 s9, s9, s11
	s_bcnt1_i32_b64 s11, s[36:37]
	s_add_i32 s9, s9, s11
	s_bcnt1_i32_b64 s11, s[38:39]
	s_add_i32 s9, s9, s11
	s_cmpk_gt_u32 s9, 0xff
	s_cselect_b32 s10, s1, s10
	s_cmpk_eq_i32 s9, 0x100
	s_cbranch_scc1 .LBB0_879
	s_add_i32 s0, s0, -1
	s_cmp_eq_u32 s0, -1
	s_cbranch_scc0 .LBB0_878
